# out-GEMM epilogues of both layers de-serialised: residual/base row loads hoisted into dead K-loop operand registers (layer 0: two waves of 8 row groups), counted vmcnt waits instead of drain per row g
# speedup vs baseline: 1.0040x; 1.0040x over previous
.LBB0_981:
	s_movk_i32 s52, 0x7f
	v_lshl_add_u32 v124, v122, 8, v173
	v_cmp_lt_i32_e32 vcc, s52, v122
	v_ashrrev_i32_e32 v125, 31, v124
	s_and_saveexec_b64 s[52:53], vcc
	s_xor_b64 s[52:53], exec, s[52:53]
	v_lshlrev_b64 v[122:123], 12, v[124:125]
	s_brev_b32 s54, 31
	v_lshl_add_u64 v[122:123], s[20:21], 0, v[122:123]
	s_mov_b32 s55, -1
	v_lshl_add_u64 v[126:127], v[122:123], 0, s[54:55]
	s_or_saveexec_b64 s[52:53], s[52:53]
	v_mov_b64_e32 v[132:133], 0xc000
	s_xor_b64 exec, exec, s[52:53]
	v_lshrrev_b32_e32 v121, 4, v122
	s_movk_i32 s54, 0x1800
	v_mul_lo_u32 v132, v121, s54
	v_lshlrev_b64 v[122:123], 12, v[124:125]
	v_lshl_add_u64 v[126:127], s[18:19], 0, v[122:123]
	v_ashrrev_i32_e32 v133, 31, v132
	s_or_b64 exec, exec, s[52:53]
	v_lshl_or_b32 v120, v120, 8, v174
	v_ashrrev_i32_e32 v121, 31, v120
	v_lshl_add_u64 v[122:123], v[132:133], 2, s[30:31]
	v_lshlrev_b64 v[132:133], 2, v[120:121]
	v_lshl_add_u64 v[170:171], v[126:127], 0, v[132:133]
	v_lshl_add_u64 v[186:187], v[122:123], 0, v[132:133]
	global_load_dwordx4 v[178:181], v[170:171], off
	global_load_dwordx4 v[136:139], v[186:187], off
	global_load_dwordx4 v[132:135], v[186:187], off offset:16
	global_load_dwordx4 v[182:185], v[170:171], off offset:16
	v_lshlrev_b64 v[122:123], 11, v[124:125]
	v_lshl_add_u64 v[122:123], s[28:29], 0, v[122:123]
	v_lshl_add_u64 v[168:169], v[120:121], 1, v[122:123]
	global_load_dwordx4 v[120:123], v[186:187], off offset:528
	global_load_dwordx4 v[124:127], v[186:187], off offset:512
	global_load_dwordx4 v[188:191], v[170:171], off offset:512
	global_load_dwordx4 v[192:195], v[170:171], off offset:528
	s_mov_b32 s98, 0x10000
	s_mov_b32 s99, 0
	v_lshl_add_u64 v[252:253], v[170:171], 0, s[98:99]
	global_load_dwordx4 v[196:199], v[252:253], off
	global_load_dwordx4 v[200:203], v[252:253], off offset:16
	s_mov_b32 s98, 0x10000
	s_mov_b32 s99, 0
	v_lshl_add_u64 v[252:253], v[170:171], 0, s[98:99]
	global_load_dwordx4 v[204:207], v[252:253], off offset:512
	global_load_dwordx4 v[208:211], v[252:253], off offset:528
	s_mov_b32 s98, 0x20000
	s_mov_b32 s99, 0
	v_lshl_add_u64 v[252:253], v[170:171], 0, s[98:99]
	global_load_dwordx4 v[212:215], v[252:253], off
	global_load_dwordx4 v[216:219], v[252:253], off offset:16
	s_mov_b32 s98, 0x20000
	s_mov_b32 s99, 0
	v_lshl_add_u64 v[252:253], v[170:171], 0, s[98:99]
	global_load_dwordx4 v[220:223], v[252:253], off offset:512
	global_load_dwordx4 v[224:227], v[252:253], off offset:528
	s_mov_b32 s98, 0x30000
	s_mov_b32 s99, 0
	v_lshl_add_u64 v[252:253], v[170:171], 0, s[98:99]
	global_load_dwordx4 v[228:231], v[252:253], off
	global_load_dwordx4 v[232:235], v[252:253], off offset:16
	s_mov_b32 s98, 0x30000
	s_mov_b32 s99, 0
	v_lshl_add_u64 v[252:253], v[170:171], 0, s[98:99]
	global_load_dwordx4 v[236:239], v[252:253], off offset:512
	global_load_dwordx4 v[240:243], v[252:253], off offset:528
	s_mov_b32 s98, 0x80000
	s_mov_b32 s99, 0
	v_lshl_add_u64 v[252:253], v[170:171], 0, s[98:99]
	global_load_dwordx4 v[244:247], v[252:253], off
	global_load_dwordx4 v[248:251], v[252:253], off offset:16
	s_mov_b32 s52, 0x8000
	s_mov_b64 s[54:55], -1
	s_waitcnt vmcnt(16)
	v_pk_fma_f32 v[140:141], v[140:141], v[136:137], v[178:179]
	v_pk_fma_f32 v[142:143], v[142:143], v[138:139], v[180:181]
	v_pk_fma_f32 v[178:179], v[130:131], v[134:135], v[184:185]
	v_pk_fma_f32 v[130:131], v[128:129], v[132:133], v[182:183]
	v_cvt_pk_bf16_f32 v128, v140, v141
	v_cvt_pk_bf16_f32 v129, v142, v143
	s_nop 0
	v_cvt_pk_bf16_f32 v130, v130, v131
	v_cvt_pk_bf16_f32 v131, v178, v179
	global_store_dwordx4 v[168:169], v[128:131], off
	s_nop 0
	v_add_co_u32_e32 v178, vcc, s66, v170
	s_waitcnt vmcnt(15)
	v_pk_fma_f32 v[116:117], v[116:117], v[124:125], v[188:189]
	v_pk_fma_f32 v[128:129], v[114:115], v[122:123], v[194:195]
	v_pk_fma_f32 v[114:115], v[112:113], v[120:121], v[192:193]
	v_addc_co_u32_e32 v179, vcc, 0, v171, vcc
	v_pk_fma_f32 v[118:119], v[118:119], v[126:127], v[190:191]
	v_cvt_pk_bf16_f32 v112, v116, v117
	v_add_co_u32_e32 v130, vcc, s52, v168
	v_cvt_pk_bf16_f32 v113, v118, v119
	v_cvt_pk_bf16_f32 v114, v114, v115
	v_cvt_pk_bf16_f32 v115, v128, v129
	global_store_dwordx4 v[168:169], v[112:115], off offset:256
	v_lshl_add_u64 v[128:129], v[170:171], 0, s[44:45]
	s_mov_b32 s98, 0x80000
	s_mov_b32 s99, 0
	v_lshl_add_u64 v[252:253], v[170:171], 0, s[98:99]
	global_load_dwordx4 v[188:191], v[252:253], off offset:512
	global_load_dwordx4 v[192:195], v[252:253], off offset:528
	v_addc_co_u32_e32 v131, vcc, 0, v169, vcc
	s_mov_b64 s[52:53], 0x8000
	s_waitcnt vmcnt(16)
	v_pk_fma_f32 v[108:109], v[108:109], v[136:137], v[196:197]
	v_pk_fma_f32 v[112:113], v[106:107], v[134:135], v[202:203]
	v_pk_fma_f32 v[106:107], v[104:105], v[132:133], v[200:201]
	v_pk_fma_f32 v[110:111], v[110:111], v[138:139], v[198:199]
	v_cvt_pk_bf16_f32 v104, v108, v109
	s_nop 0
	v_cvt_pk_bf16_f32 v105, v110, v111
	v_cvt_pk_bf16_f32 v106, v106, v107
	v_cvt_pk_bf16_f32 v107, v112, v113
	global_store_dwordx4 v[130:131], v[104:107], off
	s_nop 0
	s_mov_b32 s98, 0x90000
	s_mov_b32 s99, 0
	v_lshl_add_u64 v[252:253], v[170:171], 0, s[98:99]
	global_load_dwordx4 v[196:199], v[252:253], off
	global_load_dwordx4 v[200:203], v[252:253], off offset:16
	v_lshl_add_u64 v[112:113], v[168:169], 0, s[52:53]
	s_mov_b32 s52, 0x20000
	v_add_co_u32_e32 v114, vcc, s52, v170
	s_mov_b64 s[52:53], 0x20000
	s_nop 0
	v_addc_co_u32_e32 v115, vcc, 0, v171, vcc
	s_waitcnt vmcnt(17)
	v_pk_fma_f32 v[100:101], v[100:101], v[124:125], v[204:205]
	v_pk_fma_f32 v[104:105], v[98:99], v[122:123], v[210:211]
	v_pk_fma_f32 v[98:99], v[96:97], v[120:121], v[208:209]
	v_pk_fma_f32 v[102:103], v[102:103], v[126:127], v[206:207]
	v_cvt_pk_bf16_f32 v96, v100, v101
	v_add_co_u32_e32 v106, vcc, s66, v168
	v_cvt_pk_bf16_f32 v97, v102, v103
	v_cvt_pk_bf16_f32 v98, v98, v99
	v_cvt_pk_bf16_f32 v99, v104, v105
	global_store_dwordx4 v[112:113], v[96:99], off offset:256
	v_lshl_add_u64 v[104:105], v[170:171], 0, s[52:53]
	s_mov_b32 s98, 0x90000
	s_mov_b32 s99, 0
	v_lshl_add_u64 v[252:253], v[170:171], 0, s[98:99]
	global_load_dwordx4 v[204:207], v[252:253], off offset:512
	global_load_dwordx4 v[208:211], v[252:253], off offset:528
	v_addc_co_u32_e32 v107, vcc, 0, v169, vcc
	s_mov_b32 s52, 0x30000
	s_waitcnt vmcnt(18)
	v_pk_fma_f32 v[92:93], v[92:93], v[136:137], v[212:213]
	v_pk_fma_f32 v[96:97], v[90:91], v[134:135], v[218:219]
	v_pk_fma_f32 v[90:91], v[88:89], v[132:133], v[216:217]
	v_pk_fma_f32 v[94:95], v[94:95], v[138:139], v[214:215]
	v_cvt_pk_bf16_f32 v88, v92, v93
	v_add_co_u32_e32 v98, vcc, s52, v170
	v_cvt_pk_bf16_f32 v89, v94, v95
	v_cvt_pk_bf16_f32 v90, v90, v91
	v_cvt_pk_bf16_f32 v91, v96, v97
	global_store_dwordx4 v[106:107], v[88:91], off
	s_nop 0
	s_mov_b32 s98, 0xa0000
	s_mov_b32 s99, 0
	v_lshl_add_u64 v[252:253], v[170:171], 0, s[98:99]
	global_load_dwordx4 v[212:215], v[252:253], off
	global_load_dwordx4 v[216:219], v[252:253], off offset:16
	v_lshl_add_u64 v[96:97], v[168:169], 0, s[44:45]
	s_mov_b64 s[52:53], 0x30000
	v_addc_co_u32_e32 v99, vcc, 0, v171, vcc
	s_waitcnt vmcnt(19)
	v_pk_fma_f32 v[84:85], v[84:85], v[124:125], v[220:221]
	v_pk_fma_f32 v[88:89], v[82:83], v[122:123], v[226:227]
	v_pk_fma_f32 v[82:83], v[80:81], v[120:121], v[224:225]
	v_pk_fma_f32 v[86:87], v[86:87], v[126:127], v[222:223]
	v_cvt_pk_bf16_f32 v80, v84, v85
	s_nop 0
	v_cvt_pk_bf16_f32 v81, v86, v87
	v_cvt_pk_bf16_f32 v82, v82, v83
	v_cvt_pk_bf16_f32 v83, v88, v89
	global_store_dwordx4 v[96:97], v[80:83], off offset:256
	v_lshl_add_u64 v[88:89], v[170:171], 0, s[52:53]
	s_mov_b32 s98, 0xa0000
	s_mov_b32 s99, 0
	v_lshl_add_u64 v[252:253], v[170:171], 0, s[98:99]
	global_load_dwordx4 v[220:223], v[252:253], off offset:512
	global_load_dwordx4 v[224:227], v[252:253], off offset:528
	s_mov_b32 s52, 0x18000
	v_add_co_u32_e32 v90, vcc, s52, v168
	s_mov_b64 s[52:53], 0x18000
	s_nop 0
	v_addc_co_u32_e32 v91, vcc, 0, v169, vcc
	s_waitcnt vmcnt(20)
	v_pk_fma_f32 v[76:77], v[76:77], v[136:137], v[228:229]
	v_pk_fma_f32 v[80:81], v[74:75], v[134:135], v[234:235]
	v_pk_fma_f32 v[74:75], v[72:73], v[132:133], v[232:233]
	v_pk_fma_f32 v[78:79], v[78:79], v[138:139], v[230:231]
	v_cvt_pk_bf16_f32 v72, v76, v77
	s_nop 0
	v_cvt_pk_bf16_f32 v73, v78, v79
	v_cvt_pk_bf16_f32 v74, v74, v75
	v_cvt_pk_bf16_f32 v75, v80, v81
	global_store_dwordx4 v[90:91], v[72:75], off
	s_nop 0
	s_mov_b32 s98, 0xb0000
	s_mov_b32 s99, 0
	v_lshl_add_u64 v[252:253], v[170:171], 0, s[98:99]
	global_load_dwordx4 v[228:231], v[252:253], off
	global_load_dwordx4 v[232:235], v[252:253], off offset:16
	v_lshl_add_u64 v[80:81], v[168:169], 0, s[52:53]
	s_mov_b32 s52, 0x80000
	v_add_co_u32_e32 v82, vcc, s52, v170
	s_mov_b64 s[52:53], 0x80000
	s_nop 0
	v_addc_co_u32_e32 v83, vcc, 0, v171, vcc
	s_waitcnt vmcnt(21)
	v_pk_fma_f32 v[68:69], v[68:69], v[124:125], v[236:237]
	v_pk_fma_f32 v[72:73], v[66:67], v[122:123], v[242:243]
	v_pk_fma_f32 v[66:67], v[64:65], v[120:121], v[240:241]
	v_pk_fma_f32 v[70:71], v[70:71], v[126:127], v[238:239]
	v_cvt_pk_bf16_f32 v64, v68, v69
	s_nop 0
	v_cvt_pk_bf16_f32 v65, v70, v71
	v_cvt_pk_bf16_f32 v66, v66, v67
	v_cvt_pk_bf16_f32 v67, v72, v73
	global_store_dwordx4 v[80:81], v[64:67], off offset:256
	v_lshl_add_u64 v[72:73], v[170:171], 0, s[52:53]
	s_mov_b32 s98, 0xb0000
	s_mov_b32 s99, 0
	v_lshl_add_u64 v[252:253], v[170:171], 0, s[98:99]
	global_load_dwordx4 v[236:239], v[252:253], off offset:512
	global_load_dwordx4 v[240:243], v[252:253], off offset:528
	s_mov_b32 s52, 0x40000
	v_add_co_u32_e32 v74, vcc, s52, v168
	s_mov_b32 s52, 0x90000
	s_nop 0
	v_addc_co_u32_e32 v75, vcc, 0, v169, vcc
	s_waitcnt vmcnt(22)
	v_pk_fma_f32 v[60:61], v[60:61], v[136:137], v[244:245]
	v_pk_fma_f32 v[64:65], v[58:59], v[134:135], v[250:251]
	v_pk_fma_f32 v[58:59], v[56:57], v[132:133], v[248:249]
	v_pk_fma_f32 v[62:63], v[62:63], v[138:139], v[246:247]
	v_cvt_pk_bf16_f32 v56, v60, v61
	v_add_co_u32_e32 v66, vcc, s52, v170
	v_cvt_pk_bf16_f32 v57, v62, v63
	v_cvt_pk_bf16_f32 v58, v58, v59
	v_cvt_pk_bf16_f32 v59, v64, v65
	global_store_dwordx4 v[74:75], v[56:59], off
	s_nop 0
	v_lshl_add_u64 v[64:65], v[168:169], 0, s[10:11]
	s_mov_b64 s[52:53], 0x90000
	v_addc_co_u32_e32 v67, vcc, 0, v171, vcc
	s_waitcnt vmcnt(19)
	v_pk_fma_f32 v[52:53], v[52:53], v[124:125], v[188:189]
	v_pk_fma_f32 v[56:57], v[50:51], v[122:123], v[194:195]
	v_pk_fma_f32 v[50:51], v[48:49], v[120:121], v[192:193]
	v_pk_fma_f32 v[54:55], v[54:55], v[126:127], v[190:191]
	v_cvt_pk_bf16_f32 v48, v52, v53
	s_nop 0
	v_cvt_pk_bf16_f32 v49, v54, v55
	v_cvt_pk_bf16_f32 v50, v50, v51
	v_cvt_pk_bf16_f32 v51, v56, v57
	global_store_dwordx4 v[64:65], v[48:51], off offset:256
	v_lshl_add_u64 v[56:57], v[170:171], 0, s[52:53]
	s_mov_b32 s52, 0x48000
	v_add_co_u32_e32 v58, vcc, s52, v168
	s_mov_b64 s[52:53], 0x48000
	s_nop 0
	v_addc_co_u32_e32 v59, vcc, 0, v169, vcc
	s_waitcnt vmcnt(17)
	v_pk_fma_f32 v[44:45], v[44:45], v[136:137], v[196:197]
	v_pk_fma_f32 v[48:49], v[42:43], v[134:135], v[202:203]
	v_pk_fma_f32 v[42:43], v[40:41], v[132:133], v[200:201]
	v_pk_fma_f32 v[46:47], v[46:47], v[138:139], v[198:199]
	v_cvt_pk_bf16_f32 v40, v44, v45
	v_add_co_u32_e32 v50, vcc, s92, v170
	v_cvt_pk_bf16_f32 v41, v46, v47
	v_cvt_pk_bf16_f32 v42, v42, v43
	v_cvt_pk_bf16_f32 v43, v48, v49
	global_store_dwordx4 v[58:59], v[40:43], off
	s_nop 0
	v_lshl_add_u64 v[48:49], v[168:169], 0, s[52:53]
	v_addc_co_u32_e32 v51, vcc, 0, v171, vcc
	s_mov_b64 s[52:53], 0x50000
	s_waitcnt vmcnt(15)
	v_pk_fma_f32 v[36:37], v[36:37], v[124:125], v[204:205]
	v_pk_fma_f32 v[40:41], v[34:35], v[122:123], v[210:211]
	v_pk_fma_f32 v[34:35], v[32:33], v[120:121], v[208:209]
	v_pk_fma_f32 v[38:39], v[38:39], v[126:127], v[206:207]
	v_cvt_pk_bf16_f32 v32, v36, v37
	v_add_co_u32_e32 v42, vcc, s93, v168
	v_cvt_pk_bf16_f32 v33, v38, v39
	v_cvt_pk_bf16_f32 v34, v34, v35
	v_cvt_pk_bf16_f32 v35, v40, v41
	global_store_dwordx4 v[48:49], v[32:35], off offset:256
	v_lshl_add_u64 v[40:41], v[170:171], 0, s[46:47]
	v_addc_co_u32_e32 v43, vcc, 0, v169, vcc
	s_waitcnt vmcnt(13)
	v_pk_fma_f32 v[28:29], v[28:29], v[136:137], v[212:213]
	v_pk_fma_f32 v[32:33], v[26:27], v[134:135], v[218:219]
	v_pk_fma_f32 v[26:27], v[24:25], v[132:133], v[216:217]
	v_pk_fma_f32 v[30:31], v[30:31], v[138:139], v[214:215]
	v_cvt_pk_bf16_f32 v24, v28, v29
	v_add_co_u32_e32 v34, vcc, s94, v170
	v_cvt_pk_bf16_f32 v25, v30, v31
	v_cvt_pk_bf16_f32 v26, v26, v27
	v_cvt_pk_bf16_f32 v27, v32, v33
	global_store_dwordx4 v[42:43], v[24:27], off
	s_nop 0
	v_lshl_add_u64 v[32:33], v[168:169], 0, s[52:53]
	v_addc_co_u32_e32 v35, vcc, 0, v171, vcc
	s_waitcnt vmcnt(11)
	v_pk_fma_f32 v[20:21], v[20:21], v[124:125], v[220:221]
	v_pk_fma_f32 v[24:25], v[18:19], v[122:123], v[226:227]
	v_pk_fma_f32 v[18:19], v[16:17], v[120:121], v[224:225]
	v_pk_fma_f32 v[22:23], v[22:23], v[126:127], v[222:223]
	v_cvt_pk_bf16_f32 v16, v20, v21
	v_add_co_u32_e32 v26, vcc, s95, v168
	v_cvt_pk_bf16_f32 v17, v22, v23
	v_cvt_pk_bf16_f32 v18, v18, v19
	v_cvt_pk_bf16_f32 v19, v24, v25
	global_store_dwordx4 v[32:33], v[16:19], off offset:256
	v_lshl_add_u64 v[24:25], v[170:171], 0, s[50:51]
	v_addc_co_u32_e32 v27, vcc, 0, v169, vcc
	s_waitcnt vmcnt(9)
	v_pk_fma_f32 v[12:13], v[12:13], v[136:137], v[228:229]
	v_pk_fma_f32 v[16:17], v[10:11], v[134:135], v[234:235]
	v_pk_fma_f32 v[10:11], v[8:9], v[132:133], v[232:233]
	v_pk_fma_f32 v[14:15], v[14:15], v[138:139], v[230:231]
	v_cvt_pk_bf16_f32 v8, v12, v13
	s_nop 0
	v_cvt_pk_bf16_f32 v9, v14, v15
	v_cvt_pk_bf16_f32 v10, v10, v11
	v_cvt_pk_bf16_f32 v11, v16, v17
	global_store_dwordx4 v[26:27], v[8:11], off
	s_nop 0
	v_lshl_add_u64 v[16:17], v[168:169], 0, s[48:49]
	s_waitcnt vmcnt(7)
	v_pk_fma_f32 v[4:5], v[4:5], v[124:125], v[236:237]
	v_pk_fma_f32 v[8:9], v[2:3], v[122:123], v[242:243]
	v_pk_fma_f32 v[2:3], v[0:1], v[120:121], v[240:241]
	v_pk_fma_f32 v[6:7], v[6:7], v[126:127], v[238:239]
	v_cvt_pk_bf16_f32 v0, v4, v5
	s_nop 0
	v_cvt_pk_bf16_f32 v1, v6, v7
	v_cvt_pk_bf16_f32 v2, v2, v3
	v_cvt_pk_bf16_f32 v3, v8, v9
	global_store_dwordx4 v[16:17], v[0:3], off offset:256
	s_and_saveexec_b64 s[52:53], s[2:3]
	s_cbranch_execz .LBB0_970
	s_andn2_b64 vcc, exec, s[12:13]
	s_cbranch_vccnz .LBB0_969
	s_barrier
	s_branch .LBB0_969
